# cross-attention: K/V loads of key tiles 1..3 all requested in the unit prologue (own staging registers, rotated per tile) instead of one tile ahead
# baseline (speedup 1.0000x reference)
.LBB0_1266:
	s_lshl_b32 s4, s19, 1
	s_ashr_i32 s21, s8, 5
	s_and_b32 s22, s8, 7
	s_and_b32 s28, s4, 0x180
	s_lshl_b32 s4, s21, 11
	s_lshl_b32 s5, s22, 8
	s_or_b32 s6, s4, s5
	s_ashr_i32 s7, s6, 31
	s_lshl_b64 s[4:5], s[6:7], 8
	s_lshl_b64 s[6:7], s[6:7], 9
	s_add_u32 s6, s10, s6
	s_addc_u32 s7, s11, s7
	s_lshl_b32 s23, s8, 3
	s_and_b32 s23, s23, 0xc0
	s_lshl_b32 s26, s23, 1
	s_add_u32 s24, s6, s26
	s_addc_u32 s25, s7, 0
	s_lshl_b32 s6, s21, 8
	s_ashr_i32 s7, s6, 31
	s_lshl_b64 s[6:7], s[6:7], 10
	s_add_u32 s27, s14, s6
	s_addc_u32 s29, s15, s7
	s_add_u32 s26, s27, s26
	v_mov_b32_e32 v44, v89
	s_addc_u32 s27, s29, 0
	s_movk_i32 s31, 0xffe0
	v_readfirstlane_b32 s29, v44
	s_ashr_i32 s30, s29, 1
	v_mov_b32_e32 v0, s30
	v_bfi_b32 v0, s31, v0, v44
	v_ashrrev_i32_e32 v1, 31, v0
	v_bfe_u32 v45, v44, 5, 1
	v_lshlrev_b64 v[0:1], 9, v[0:1]
	v_lshl_add_u64 v[0:1], s[24:25], 0, v[0:1]
	v_lshlrev_b32_e32 v208, 4, v45
	v_lshl_add_u64 v[0:1], v[0:1], 0, v[208:209]
	global_load_dwordx4 v[76:79], v[0:1], off
	global_load_dwordx4 v[72:75], v[0:1], off offset:32
	global_load_dwordx4 v[68:71], v[0:1], off offset:64
	global_load_dwordx4 v[64:67], v[0:1], off offset:96
	v_ashrrev_i32_e32 v1, 31, v44
	v_lshrrev_b32_e32 v1, 29, v1
	v_add_u32_e32 v1, v44, v1
	v_ashrrev_i32_e32 v2, 3, v1
	v_and_b32_e32 v1, -8, v1
	v_sub_u32_e32 v1, v44, v1
	v_ashrrev_i32_e32 v3, 31, v2
	v_lshlrev_b32_e32 v6, 3, v1
	v_lshlrev_b64 v[40:41], 10, v[2:3]
	v_ashrrev_i32_e32 v7, 31, v6
	v_lshl_add_u64 v[4:5], s[26:27], 0, v[40:41]
	v_lshlrev_b64 v[42:43], 1, v[6:7]
	v_mov_b32_e32 v0, v209
	v_mov_b32_e32 v16, v209
	v_lshl_add_u64 v[4:5], v[4:5], 0, v[42:43]
	global_load_dwordx4 v[32:35], v[4:5], off
	global_load_dwordx4 v[36:39], v[4:5], off offset:512
	v_lshl_add_u64 v[138:139], v[40:41], 0, s[6:7]
	v_or_b32_e32 v138, s28, v138
	v_lshl_add_u64 v[138:139], v[138:139], 0, v[42:43]
	v_lshl_add_u64 v[136:137], s[2:3], 0, v[138:139]
	global_load_dwordx4 v[84:87], v[136:137], off offset:-512
	global_load_dwordx4 v[80:83], v[136:137], off
	v_lshl_add_u64 v[136:137], v[136:137], 0, s[74:75]
	global_load_dwordx4 v[120:123], v[136:137], off offset:-512
	global_load_dwordx4 v[124:127], v[136:137], off
	v_lshl_add_u64 v[136:137], v[136:137], 0, s[74:75]
	global_load_dwordx4 v[128:131], v[136:137], off offset:-512
	global_load_dwordx4 v[132:135], v[136:137], off
	s_movk_i32 s24, 0x90
	v_mul_lo_u32 v3, v2, s24
	v_lshlrev_b32_e32 v1, 4, v1
	v_and_b32_e32 v46, 31, v44
	v_add3_u32 v88, 0, v3, v1
	v_mad_u64_u32 v[90:91], s[24:25], v2, 48, v[88:89]
	s_and_b32 s25, s29, 0x3fffffc0
	s_lshl_b32 s25, s25, 2
	v_and_b32_e32 v96, 63, v44
	s_add_i32 s25, s25, 0
	s_mov_b32 s26, 0
	s_and_b32 s24, s30, 0xffffffe0
	v_mov_b32_e32 v1, v0
	v_mov_b32_e32 v2, v0
	v_mov_b32_e32 v3, v0
	v_mov_b32_e32 v4, v0
	v_mov_b32_e32 v5, v0
	v_mov_b32_e32 v6, v0
	v_mov_b32_e32 v7, v0
	v_mov_b32_e32 v8, v0
	v_mov_b32_e32 v9, v0
	v_mov_b32_e32 v10, v0
	v_mov_b32_e32 v11, v0
	v_mov_b32_e32 v12, v0
	v_mov_b32_e32 v13, v0
	v_mov_b32_e32 v14, v0
	v_mov_b32_e32 v15, v0
	v_mov_b32_e32 v17, v16
	v_mov_b32_e32 v18, v16
	v_mov_b32_e32 v19, v16
	v_mov_b32_e32 v20, v16
	v_mov_b32_e32 v21, v16
	v_mov_b32_e32 v22, v16
	v_mov_b32_e32 v23, v16
	v_mov_b32_e32 v24, v16
	v_mov_b32_e32 v25, v16
	v_mov_b32_e32 v26, v16
	v_mov_b32_e32 v27, v16
	v_mov_b32_e32 v28, v16
	v_mov_b32_e32 v29, v16
	v_mov_b32_e32 v30, v16
	v_mov_b32_e32 v31, v16
	v_lshl_add_u32 v98, v96, 2, s25
	v_add_u32_e32 v97, s25, v208
	v_mov_b32_e32 v100, 0xff800000
	v_mov_b32_e32 v103, 0
	s_waitcnt vmcnt(7)
	ds_write_b128 v88, v[32:35]
	s_waitcnt vmcnt(6)
	ds_write_b128 v90, v[36:39] offset:18432
	v_mul_u32_u24_e32 v32, 0x90, v46
	v_add3_u32 v101, 0, v32, v208
	v_bfe_u32 v32, v44, 2, 2
	v_and_b32_e32 v33, 16, v44
	v_lshlrev_b32_e32 v34, 2, v44
	v_lshl_or_b32 v32, v45, 2, v32
	v_and_or_b32 v33, v34, 12, v33
	v_mul_u32_u24_e32 v32, 0xc0, v32
	v_lshlrev_b32_e32 v33, 1, v33
	v_add3_u32 v91, 0, v32, v33
	v_lshl_add_u64 v[32:33], v[40:41], 0, s[6:7]
	v_or_b32_e32 v32, s28, v32
	v_lshl_add_u64 v[32:33], v[32:33], 0, v[42:43]
	v_lshl_add_u64 v[92:93], s[2:3], 0, v[32:33]
	s_waitcnt lgkmcnt(0)
	s_barrier
.LBB0_1267:
	s_and_b32 s6, s26, 1
	s_mul_i32 s7, s6, 0x2400
	v_mov_b32_e32 v32, 0
	v_add_u32_e32 v94, s7, v101
	ds_read_b128 v[104:107], v94
	ds_read_b128 v[108:111], v94 offset:4608
	v_mov_b32_e32 v33, v32
	v_mov_b32_e32 v34, v32
	v_mov_b32_e32 v35, v32
	v_mov_b32_e32 v36, v32
	v_mov_b32_e32 v37, v32
	v_mov_b32_e32 v38, v32
	v_mov_b32_e32 v39, v32
	v_mov_b32_e32 v40, v32
	v_mov_b32_e32 v41, v32
	v_mov_b32_e32 v42, v32
	v_mov_b32_e32 v43, v32
	v_mov_b32_e32 v44, v32
	v_mov_b32_e32 v45, v32
	v_mov_b32_e32 v46, v32
	v_mov_b32_e32 v47, v32
	v_and_b32_e32 v95, 64, v225
	v_add_u32_e32 v95, 64, v95
	s_waitcnt lgkmcnt(1)
	v_mfma_f32_32x32x16_bf16 v[48:63], v[104:107], v[76:79], v[32:47]
	ds_read_b128 v[104:107], v94 offset:32
	s_waitcnt lgkmcnt(1)
	v_mfma_f32_32x32x16_bf16 v[32:47], v[108:111], v[76:79], v[32:47]
	ds_read_b128 v[108:111], v94 offset:4640
	s_waitcnt lgkmcnt(1)
	v_mfma_f32_32x32x16_bf16 v[48:63], v[104:107], v[72:75], v[48:63]
	ds_read_b128 v[104:107], v94 offset:64
	s_waitcnt lgkmcnt(1)
	v_mfma_f32_32x32x16_bf16 v[32:47], v[108:111], v[72:75], v[32:47]
	ds_read_b128 v[108:111], v94 offset:4672
	s_waitcnt lgkmcnt(1)
	v_mfma_f32_32x32x16_bf16 v[48:63], v[104:107], v[68:71], v[48:63]
	ds_read_b128 v[104:107], v94 offset:96
	s_waitcnt lgkmcnt(1)
	v_mfma_f32_32x32x16_bf16 v[32:47], v[108:111], v[68:71], v[32:47]
	ds_read_b128 v[108:111], v94 offset:4704
	v_xor_b32_e32 v94, 32, v225
	v_cmp_lt_i32_e32 vcc, v94, v95
	s_nop 1
	v_cndmask_b32_e32 v94, v225, v94, vcc
	v_lshlrev_b32_e32 v102, 2, v94
	s_waitcnt lgkmcnt(1)
	v_mfma_f32_32x32x16_bf16 v[48:63], v[104:107], v[64:67], v[48:63]
	s_waitcnt lgkmcnt(0)
	v_mfma_f32_32x32x16_bf16 v[32:47], v[108:111], v[64:67], v[32:47]
	s_nop 9
	v_max_f32_e32 v95, v49, v49
	v_max_f32_e32 v99, v48, v48
	v_max_f32_e32 v95, v99, v95
	v_max3_f32 v99, v50, v51, v33
	v_max3_f32 v95, v95, v32, v34
	v_max3_f32 v95, v95, v35, v52
	v_max3_f32 v99, v99, v54, v55
	v_max3_f32 v95, v95, v53, v36
	v_max3_f32 v99, v99, v38, v39
	v_max3_f32 v95, v95, v37, v56
	v_max3_f32 v99, v99, v58, v59
	v_max3_f32 v95, v95, v57, v40
	v_max3_f32 v99, v99, v42, v43
	v_max3_f32 v95, v95, v41, v60
	v_max3_f32 v99, v99, v62, v63
	v_max3_f32 v95, v95, v61, v44
	v_max3_f32 v99, v99, v46, v47
	v_max3_f32 v94, v95, v45, v99
	ds_bpermute_b32 v95, v102, v94
	s_waitcnt lgkmcnt(0)
	v_max_f32_e32 v95, v95, v95
	v_max_f32_e32 v94, v94, v95
	v_mov_b32_e32 v95, v100
	v_add_f32_e32 v94, 0, v94
	v_max_f32_e32 v99, v95, v95
	v_max_f32_e32 v100, v99, v94
	v_sub_f32_e32 v48, v48, v100
	v_sub_f32_e32 v32, v32, v100
	v_sub_f32_e32 v99, v95, v100
	v_exp_f32_e32 v94, v48
	v_exp_f32_e32 v95, v32
	v_sub_f32_e32 v32, v49, v100
	v_sub_f32_e32 v33, v33, v100
	v_exp_f32_e32 v32, v32
	v_exp_f32_e32 v33, v33
	v_sub_f32_e32 v48, v50, v100
	v_sub_f32_e32 v34, v34, v100
	v_exp_f32_e32 v48, v48
	v_exp_f32_e32 v49, v34
	v_sub_f32_e32 v34, v51, v100
	v_sub_f32_e32 v35, v35, v100
	v_exp_f32_e32 v34, v34
	v_exp_f32_e32 v35, v35
	v_pk_add_f32 v[50:51], v[94:95], 0 op_sel_hi:[1,0]
	v_sub_f32_e32 v36, v36, v100
	v_pk_add_f32 v[50:51], v[32:33], v[50:51]
	v_sub_f32_e32 v37, v37, v100
	v_pk_add_f32 v[50:51], v[48:49], v[50:51]
	v_exp_f32_e32 v37, v37
	v_pk_add_f32 v[104:105], v[34:35], v[50:51]
	v_sub_f32_e32 v50, v52, v100
	v_exp_f32_e32 v50, v50
	v_exp_f32_e32 v51, v36
	v_sub_f32_e32 v36, v53, v100
	v_exp_f32_e32 v36, v36
	v_sub_f32_e32 v52, v54, v100
	v_sub_f32_e32 v38, v38, v100
	v_exp_f32_e32 v52, v52
	v_exp_f32_e32 v53, v38
	v_sub_f32_e32 v38, v55, v100
	v_sub_f32_e32 v39, v39, v100
	v_exp_f32_e32 v38, v38
	v_exp_f32_e32 v39, v39
	v_sub_f32_e32 v54, v56, v100
	v_sub_f32_e32 v40, v40, v100
	v_sub_f32_e32 v42, v42, v100
	v_sub_f32_e32 v44, v44, v100
	v_sub_f32_e32 v46, v46, v100
	v_exp_f32_e32 v54, v54
	v_exp_f32_e32 v55, v40
	v_sub_f32_e32 v40, v57, v100
	v_sub_f32_e32 v41, v41, v100
	v_sub_f32_e32 v56, v58, v100
	v_exp_f32_e32 v57, v42
	v_sub_f32_e32 v42, v59, v100
	v_sub_f32_e32 v58, v60, v100
	v_exp_f32_e32 v59, v44
	v_sub_f32_e32 v44, v61, v100
	v_sub_f32_e32 v60, v62, v100
	v_exp_f32_e32 v61, v46
	v_sub_f32_e32 v46, v63, v100
	v_pk_add_f32 v[62:63], v[50:51], v[104:105]
	v_exp_f32_e32 v40, v40
	v_exp_f32_e32 v41, v41
	v_pk_add_f32 v[62:63], v[36:37], v[62:63]
	v_exp_f32_e32 v56, v56
	v_sub_f32_e32 v43, v43, v100
	v_pk_add_f32 v[62:63], v[52:53], v[62:63]
	v_exp_f32_e32 v42, v42
	v_exp_f32_e32 v43, v43
	v_pk_add_f32 v[62:63], v[38:39], v[62:63]
	v_exp_f32_e32 v58, v58
	v_sub_f32_e32 v45, v45, v100
	v_pk_add_f32 v[62:63], v[54:55], v[62:63]
	v_exp_f32_e32 v44, v44
	v_exp_f32_e32 v45, v45
	v_pk_add_f32 v[62:63], v[40:41], v[62:63]
	v_exp_f32_e32 v60, v60
	v_sub_f32_e32 v47, v47, v100
	v_pk_add_f32 v[62:63], v[56:57], v[62:63]
	v_exp_f32_e32 v46, v46
	v_exp_f32_e32 v47, v47
	v_pk_add_f32 v[62:63], v[42:43], v[62:63]
	s_nop 0
	v_pk_add_f32 v[62:63], v[58:59], v[62:63]
	s_nop 0
	v_pk_add_f32 v[62:63], v[44:45], v[62:63]
	s_nop 0
	v_pk_add_f32 v[62:63], v[60:61], v[62:63]
	s_nop 0
	v_pk_add_f32 v[104:105], v[46:47], v[62:63]
	v_exp_f32_e32 v62, v99
	v_add_f32_e32 v63, v104, v105
	ds_bpermute_b32 v99, v102, v63
	v_cmp_neq_f32_e32 vcc, 1.0, v62
	s_cbranch_vccz .LBB0_1269
	ds_write_b32 v98, v62 offset:43008
	ds_read_b128 v[104:107], v97 offset:43104
	ds_read_b128 v[108:111], v97 offset:43072
	ds_read_b128 v[112:115], v97 offset:43040
	ds_read_b128 v[116:119], v97 offset:43008
	s_waitcnt lgkmcnt(3)
	v_pk_mul_f32 v[14:15], v[106:107], v[14:15]
	s_waitcnt lgkmcnt(2)
	v_pk_mul_f32 v[10:11], v[110:111], v[10:11]
	s_waitcnt lgkmcnt(1)
	v_pk_mul_f32 v[6:7], v[114:115], v[6:7]
	s_waitcnt lgkmcnt(0)
	v_pk_mul_f32 v[2:3], v[118:119], v[2:3]
	v_pk_mul_f32 v[12:13], v[104:105], v[12:13]
	v_pk_mul_f32 v[8:9], v[108:109], v[8:9]
	v_pk_mul_f32 v[4:5], v[112:113], v[4:5]
	v_pk_mul_f32 v[0:1], v[116:117], v[0:1]
	v_pk_mul_f32 v[30:31], v[106:107], v[30:31]
	v_pk_mul_f32 v[26:27], v[110:111], v[26:27]
	v_pk_mul_f32 v[22:23], v[114:115], v[22:23]
	v_pk_mul_f32 v[18:19], v[118:119], v[18:19]
	v_pk_mul_f32 v[28:29], v[104:105], v[28:29]
	v_pk_mul_f32 v[24:25], v[108:109], v[24:25]
	v_pk_mul_f32 v[20:21], v[112:113], v[20:21]
	v_pk_mul_f32 v[16:17], v[116:117], v[16:17]
.LBB0_1269:
	s_mulk_i32 s6, 0x3000
	v_cvt_pk_bf16_f32 v110, v58, v44
	v_add_u32_e32 v44, s6, v91
	v_cvt_pk_bf16_f32 v104, v94, v32
	v_cvt_pk_bf16_f32 v105, v48, v34
	v_cvt_pk_bf16_f32 v106, v50, v36
	v_cvt_pk_bf16_f32 v107, v52, v38
	v_cvt_pk_bf16_f32 v108, v54, v40
	v_cvt_pk_bf16_f32 v109, v56, v42
	v_cvt_pk_bf16_f32 v34, v51, v37
	v_cvt_pk_bf16_f32 v36, v55, v41
	v_cvt_pk_bf16_f32 v37, v57, v43
	v_cvt_pk_bf16_f32 v111, v60, v46
	v_cvt_pk_bf16_f32 v32, v95, v33
	v_cvt_pk_bf16_f32 v33, v49, v35
	v_cvt_pk_bf16_f32 v35, v53, v39
	v_cvt_pk_bf16_f32 v38, v59, v45
	v_cvt_pk_bf16_f32 v39, v61, v47
	ds_read_b64_tr_b16 v[40:41], v44 offset:18432
	ds_read_b64_tr_b16 v[42:43], v44 offset:19968
	ds_read_b64_tr_b16 v[48:49], v44 offset:18496
	ds_read_b64_tr_b16 v[50:51], v44 offset:20032
	s_waitcnt lgkmcnt(2)
	v_mfma_f32_32x32x16_bf16 v[0:15], v[104:107], v[40:43], v[0:15]
	ds_read_b64_tr_b16 v[40:41], v44 offset:21504
	ds_read_b64_tr_b16 v[42:43], v44 offset:23040
	s_waitcnt lgkmcnt(2)
	v_mfma_f32_32x32x16_bf16 v[16:31], v[104:107], v[48:51], v[16:31]
	ds_read_b64_tr_b16 v[48:49], v44 offset:21568
	ds_read_b64_tr_b16 v[50:51], v44 offset:23104
	v_add_f32_e32 v99, v63, v99
	s_add_i32 s26, s26, 1
	v_fmac_f32_e32 v99, v103, v62
	s_waitcnt lgkmcnt(2)
	v_mfma_f32_32x32x16_bf16 v[0:15], v[108:111], v[40:43], v[0:15]
	ds_read_b64_tr_b16 v[40:41], v44 offset:24576
	ds_read_b64_tr_b16 v[42:43], v44 offset:26112
	s_waitcnt lgkmcnt(2)
	v_mfma_f32_32x32x16_bf16 v[16:31], v[108:111], v[48:51], v[16:31]
	ds_read_b64_tr_b16 v[48:49], v44 offset:24640
	ds_read_b64_tr_b16 v[50:51], v44 offset:26176
	s_waitcnt lgkmcnt(2)
	v_mfma_f32_32x32x16_bf16 v[0:15], v[32:35], v[40:43], v[0:15]
	ds_read_b64_tr_b16 v[40:41], v44 offset:27648
	ds_read_b64_tr_b16 v[42:43], v44 offset:29184
	s_waitcnt lgkmcnt(2)
	v_mfma_f32_32x32x16_bf16 v[16:31], v[32:35], v[48:51], v[16:31]
	ds_read_b64_tr_b16 v[48:49], v44 offset:27712
	ds_read_b64_tr_b16 v[50:51], v44 offset:29248
	s_waitcnt lgkmcnt(2)
	v_mfma_f32_32x32x16_bf16 v[0:15], v[36:39], v[40:43], v[0:15]
	s_waitcnt lgkmcnt(0)
	v_mfma_f32_32x32x16_bf16 v[16:31], v[36:39], v[48:51], v[16:31]
	s_bitcmp1_b32 s26, 0
	s_cselect_b32 s6, 0x2400, 0
	v_add_u32_e32 v32, s6, v88
	s_cselect_b32 s6, 0x3000, 0
	s_waitcnt vmcnt(0)
	ds_write_b128 v32, v[84:87]
	v_add_u32_e32 v32, s6, v90
	s_cmp_eq_u32 s26, 3
	v_lshl_add_u64 v[92:93], v[92:93], 0, s[74:75]
	s_waitcnt vmcnt(0)
	ds_write_b128 v32, v[80:83] offset:18432
	s_waitcnt lgkmcnt(0)
	v_mov_b64_e32 v[84:85], v[120:121]
	v_mov_b64_e32 v[86:87], v[122:123]
	v_mov_b64_e32 v[80:81], v[124:125]
	v_mov_b64_e32 v[82:83], v[126:127]
	v_mov_b64_e32 v[120:121], v[128:129]
	v_mov_b64_e32 v[122:123], v[130:131]
	v_mov_b64_e32 v[124:125], v[132:133]
	v_mov_b64_e32 v[126:127], v[134:135]
	s_barrier
	s_cbranch_scc1 .LBB0_1271
	v_mov_b32_e32 v103, v99
	s_branch .LBB0_1267
